# k_prep compose: the 5-load drain ahead of the staging loads deferred until all 32 staging loads are in flight (results in v72-v76)
# speedup vs baseline: 1.0103x; 1.0103x over previous
.LBB0_126:
	global_load_dword v72, v[4:5], off
	global_load_dword v73, v[4:5], off offset:1024
	global_load_dword v74, v[4:5], off offset:2048
	global_load_dword v75, v[4:5], off offset:3072
	v_add_co_u32_e32 v24, vcc, 0x1000, v4
	s_nop 1
	v_addc_co_u32_e32 v25, vcc, 0, v5, vcc
	v_cmp_gt_u32_e32 vcc, 0x80, v0
	s_nop 1
	s_and_saveexec_b64 s[0:1], vcc
	global_load_dword v76, v[24:25], off
	s_or_b64 exec, exec, s[0:1]
	s_waitcnt lgkmcnt(0)
	v_mov_b32_e32 v77, v3
	s_mov_b64 s[0:1], 0
	s_or_b64 exec, exec, s[0:1]
	v_or_b32_e32 v1, 0x100, v0
	v_mov_b32_e32 v8, 16
	s_mov_b64 s[0:1], 0
	v_mov_b32_e32 v7, 0
	v_mov_b32_e32 v3, v2
	v_mov_b64_e32 v[4:5], v[0:1]
	v_mov_b32_e32 v6, v4
	v_lshl_add_u64 v[24:25], v[6:7], 2, s[18:19]
	v_mov_b32_e32 v6, v5
	v_add_u32_e32 v10, 0x200, v5
	v_mov_b32_e32 v11, v7
	v_lshl_add_u64 v[26:27], v[6:7], 2, s[18:19]
	v_add_u32_e32 v6, 0x200, v4
	v_lshl_add_u64 v[10:11], v[10:11], 2, s[18:19]
	global_load_dword v1, v[24:25], off
	v_lshl_add_u64 v[24:25], v[6:7], 2, s[18:19]
	v_add_u32_e32 v6, 0x400, v4
	global_load_dword v9, v[26:27], off
	global_load_dword v28, v[24:25], off
	global_load_dword v29, v[10:11], off
	v_lshl_add_u64 v[10:11], v[6:7], 2, s[18:19]
	v_add_u32_e32 v6, 0x600, v4
	v_add_u32_e32 v12, 0x400, v5
	v_mov_b32_e32 v13, v7
	v_add_u32_e32 v14, 0x600, v5
	v_mov_b32_e32 v15, v7
	v_lshl_add_u64 v[24:25], v[6:7], 2, s[18:19]
	v_add_u32_e32 v6, 0x800, v4
	v_lshl_add_u64 v[12:13], v[12:13], 2, s[18:19]
	v_lshl_add_u64 v[14:15], v[14:15], 2, s[18:19]
	global_load_dword v26, v[10:11], off
	global_load_dword v27, v[12:13], off
	global_load_dword v30, v[24:25], off
	global_load_dword v31, v[14:15], off
	v_lshl_add_u64 v[10:11], v[6:7], 2, s[18:19]
	v_add_u32_e32 v6, 0xa00, v4
	v_add_u32_e32 v16, 0x800, v5
	v_mov_b32_e32 v17, v7
	v_add_u32_e32 v18, 0xa00, v5
	v_mov_b32_e32 v19, v7
	v_lshl_add_u64 v[12:13], v[6:7], 2, s[18:19]
	v_add_u32_e32 v6, 0xc00, v4
	v_add_u32_e32 v20, 0xc00, v5
	v_mov_b32_e32 v21, v7
	v_add_u32_e32 v22, 0xe00, v5
	v_mov_b32_e32 v23, v7
	v_lshl_add_u64 v[16:17], v[16:17], 2, s[18:19]
	v_lshl_add_u64 v[18:19], v[18:19], 2, s[18:19]
	global_load_dword v14, v[10:11], off
	global_load_dword v15, v[16:17], off
	global_load_dword v24, v[12:13], off
	global_load_dword v25, v[18:19], off
	v_lshl_add_u64 v[10:11], v[6:7], 2, s[18:19]
	v_add_u32_e32 v6, 0xe00, v4
	v_lshl_add_u64 v[20:21], v[20:21], 2, s[18:19]
	v_lshl_add_u64 v[22:23], v[22:23], 2, s[18:19]
	v_lshl_add_u64 v[12:13], v[6:7], 2, s[18:19]
	global_load_dword v6, v[10:11], off
	global_load_dword v16, v[20:21], off
	global_load_dword v17, v[12:13], off
	global_load_dword v18, v[22:23], off
	v_add_u32_e32 v5, 0x1000, v5
	v_add_u32_e32 v4, 0x1000, v4
	v_mov_b32_e32 v47, 0
	v_mov_b32_e32 v46, v4
	v_lshl_add_u64 v[64:65], v[46:47], 2, s[18:19]
	v_mov_b32_e32 v46, v5
	v_add_u32_e32 v50, 0x200, v5
	v_mov_b32_e32 v51, v47
	v_lshl_add_u64 v[66:67], v[46:47], 2, s[18:19]
	v_add_u32_e32 v46, 0x200, v4
	v_lshl_add_u64 v[50:51], v[50:51], 2, s[18:19]
	global_load_dword v41, v[64:65], off
	v_lshl_add_u64 v[64:65], v[46:47], 2, s[18:19]
	v_add_u32_e32 v46, 0x400, v4
	global_load_dword v49, v[66:67], off
	global_load_dword v68, v[64:65], off
	global_load_dword v69, v[50:51], off
	v_lshl_add_u64 v[50:51], v[46:47], 2, s[18:19]
	v_add_u32_e32 v46, 0x600, v4
	v_add_u32_e32 v52, 0x400, v5
	v_mov_b32_e32 v53, v47
	v_add_u32_e32 v54, 0x600, v5
	v_mov_b32_e32 v55, v47
	v_lshl_add_u64 v[64:65], v[46:47], 2, s[18:19]
	v_add_u32_e32 v46, 0x800, v4
	v_lshl_add_u64 v[52:53], v[52:53], 2, s[18:19]
	v_lshl_add_u64 v[54:55], v[54:55], 2, s[18:19]
	global_load_dword v66, v[50:51], off
	global_load_dword v67, v[52:53], off
	global_load_dword v70, v[64:65], off
	global_load_dword v71, v[54:55], off
	v_lshl_add_u64 v[50:51], v[46:47], 2, s[18:19]
	v_add_u32_e32 v46, 0xa00, v4
	v_add_u32_e32 v56, 0x800, v5
	v_mov_b32_e32 v57, v47
	v_add_u32_e32 v58, 0xa00, v5
	v_mov_b32_e32 v59, v47
	v_lshl_add_u64 v[52:53], v[46:47], 2, s[18:19]
	v_add_u32_e32 v46, 0xc00, v4
	v_add_u32_e32 v60, 0xc00, v5
	v_mov_b32_e32 v61, v47
	v_add_u32_e32 v62, 0xe00, v5
	v_mov_b32_e32 v63, v47
	v_lshl_add_u64 v[56:57], v[56:57], 2, s[18:19]
	v_lshl_add_u64 v[58:59], v[58:59], 2, s[18:19]
	global_load_dword v54, v[50:51], off
	global_load_dword v55, v[56:57], off
	global_load_dword v64, v[52:53], off
	global_load_dword v65, v[58:59], off
	v_lshl_add_u64 v[50:51], v[46:47], 2, s[18:19]
	v_add_u32_e32 v46, 0xe00, v4
	v_lshl_add_u64 v[60:61], v[60:61], 2, s[18:19]
	v_lshl_add_u64 v[62:63], v[62:63], 2, s[18:19]
	v_lshl_add_u64 v[52:53], v[46:47], 2, s[18:19]
	global_load_dword v46, v[50:51], off
	global_load_dword v56, v[60:61], off
	global_load_dword v57, v[52:53], off
	global_load_dword v58, v[62:63], off
	s_waitcnt vmcnt(32)
	ds_write_b32 v77, v72
	ds_write_b32 v77, v73 offset:1024
	ds_write_b32 v77, v74 offset:2048
	ds_write_b32 v77, v75 offset:3072
	v_cmp_gt_u32_e32 vcc, 0x80, v0
	s_nop 1
	s_and_saveexec_b64 s[0:1], vcc
	ds_write_b32 v77, v76 offset:4096
	s_or_b64 exec, exec, s[0:1]
	s_mov_b64 s[0:1], 0
	s_waitcnt vmcnt(30)
	ds_write2st64_b32 v3, v1, v9 offset1:4
	s_waitcnt vmcnt(28)
	ds_write2st64_b32 v3, v28, v29 offset0:8 offset1:12
	s_waitcnt vmcnt(26)
	ds_write2st64_b32 v3, v26, v27 offset0:16 offset1:20
	s_waitcnt vmcnt(24)
	ds_write2st64_b32 v3, v30, v31 offset0:24 offset1:28
	s_waitcnt vmcnt(22)
	ds_write2st64_b32 v3, v14, v15 offset0:32 offset1:36
	s_waitcnt vmcnt(20)
	ds_write2st64_b32 v3, v24, v25 offset0:40 offset1:44
	s_waitcnt vmcnt(18)
	ds_write2st64_b32 v3, v6, v16 offset0:48 offset1:52
	s_waitcnt vmcnt(16)
	ds_write2st64_b32 v3, v17, v18 offset0:56 offset1:60
	v_add_u32_e32 v3, 0x4000, v3
	s_waitcnt vmcnt(14)
	ds_write2st64_b32 v3, v41, v49 offset1:4
	s_waitcnt vmcnt(12)
	ds_write2st64_b32 v3, v68, v69 offset0:8 offset1:12
	s_waitcnt vmcnt(10)
	ds_write2st64_b32 v3, v66, v67 offset0:16 offset1:20
	s_waitcnt vmcnt(8)
	ds_write2st64_b32 v3, v70, v71 offset0:24 offset1:28
	s_waitcnt vmcnt(6)
	ds_write2st64_b32 v3, v54, v55 offset0:32 offset1:36
	s_waitcnt vmcnt(4)
	ds_write2st64_b32 v3, v64, v65 offset0:40 offset1:44
	s_waitcnt vmcnt(2)
	ds_write2st64_b32 v3, v46, v56 offset0:48 offset1:52
	s_waitcnt vmcnt(0)
	ds_write2st64_b32 v3, v57, v58 offset0:56 offset1:60
	v_add_u32_e32 v3, 0x4000, v3
	v_add_u32_e32 v5, 0x1000, v5
	v_add_u32_e32 v4, 0x1000, v4
	v_mov_b32_e32 v8, 0
	s_or_b64 exec, exec, s[0:1]
	v_mov_b32_e32 v1, 0
	v_cmp_ne_u32_e64 s[4:5], 0, 0
	s_and_saveexec_b64 s[0:1], s[4:5]
	s_cbranch_execz .LBB0_132
	s_mov_b64 s[4:5], 0
	v_mov_b32_e32 v7, 0
